# speedup vs baseline: 1.0003x; 1.0003x over previous
.LBB2_292:
	s_or_b64 exec, exec, s[0:1]
	s_movk_i32 s0, 0x224
	v_cmp_gt_u32_e64 s[0:1], s0, v0
	v_mov_b32_e32 v21, 0
	v_lshlrev_b32_e32 v48, 3, v0
	v_mov_b32_e32 v19, 0
	v_mov_b32_e32 v50, 0
	v_mov_b32_e32 v51, 0
	s_waitcnt lgkmcnt(0)
	s_and_saveexec_b64 s[6:7], s[0:1]
	s_cbranch_execz .LBB2_294
	v_mov_b32_e32 v49, 0
	v_lshl_add_u64 v[50:51], s[10:11], 0, v[48:49]
	v_add_co_u32_e32 v56, vcc, 0x1000, v50
	global_load_dwordx2 v[54:55], v48, s[10:11]
	s_nop 0
	v_addc_co_u32_e32 v57, vcc, 0, v51, vcc
	v_add_co_u32_e32 v60, vcc, 0x2000, v50
	s_movk_i32 s3, 0x5000
	s_nop 0
	v_addc_co_u32_e32 v61, vcc, 0, v51, vcc
	global_load_dwordx2 v[52:53], v[56:57], off offset:288
	global_load_dwordx2 v[58:59], v[60:61], off offset:576
	v_add_co_u32_e32 v56, vcc, 0x3000, v50
	s_movk_i32 s4, 0x7000
	s_nop 0
	v_addc_co_u32_e32 v57, vcc, 0, v51, vcc
	v_add_co_u32_e32 v60, vcc, s3, v50
	global_load_dwordx2 v[56:57], v[56:57], off offset:864
	s_nop 0
	v_addc_co_u32_e32 v61, vcc, 0, v51, vcc
	global_load_dwordx2 v[62:63], v[60:61], off offset:1440
	s_movk_i32 s3, 0x4000
	v_add_co_u32_e32 v60, vcc, s3, v50
	s_movk_i32 s3, 0x6000
	s_nop 0
	v_addc_co_u32_e32 v61, vcc, 0, v51, vcc
	v_add_co_u32_e32 v64, vcc, s3, v50
	global_load_dwordx2 v[60:61], v[60:61], off offset:1152
	s_nop 0
	v_addc_co_u32_e32 v65, vcc, 0, v51, vcc
	global_load_dwordx2 v[66:67], v[64:65], off offset:1728
	v_add_co_u32_e32 v64, vcc, s4, v50
	s_mov_b32 s8, 0x9000
	s_nop 0
	v_addc_co_u32_e32 v65, vcc, 0, v51, vcc
	global_load_dwordx2 v[68:69], v[64:65], off offset:2016
	v_add_co_u32_e32 v64, vcc, s8, v50
	s_mov_b32 s5, 0x8000
	s_nop 0
	v_addc_co_u32_e32 v65, vcc, 0, v51, vcc
	global_load_dwordx2 v[70:71], v[64:65], off offset:2592
	v_add_co_u32_e32 v64, vcc, s5, v50
	s_mov_b32 s9, 0xa000
	s_nop 0
	v_addc_co_u32_e32 v65, vcc, 0, v51, vcc
	v_add_co_u32_e32 v74, vcc, s9, v50
	global_load_dwordx2 v[72:73], v[64:65], off offset:2304
	s_nop 0
	v_addc_co_u32_e32 v75, vcc, 0, v51, vcc
	global_load_dwordx2 v[74:75], v[74:75], off offset:2880
	s_mov_b32 s10, 0xb000
	v_add_co_u32_e32 v76, vcc, s10, v50
	s_mov_b32 s11, 0x5a000
	s_nop 0
	v_addc_co_u32_e32 v77, vcc, 0, v51, vcc
	global_load_dwordx2 v[76:77], v[76:77], off offset:3168
	v_add_co_u32_e32 v64, vcc, s11, v50
	s_and_b32 s36, s2, 7
	s_mul_i32 s36, s36, 11
	s_lshr_b32 s37, s2, 3
	s_add_u32 s36, s36, s37
	s_cmp_gt_i32 s36, 0
	s_nop 0
	v_addc_co_u32_e32 v65, vcc, 0, v51, vcc
	s_cselect_b64 vcc, -1, 0
	s_cmp_gt_i32 s36, 11
	s_cselect_b64 s[4:5], -1, 0
	s_cmp_gt_i32 s36, 22
	s_mov_b32 s3, 0xd000
	global_load_dwordx2 v[64:65], v[64:65], off offset:4000
	s_waitcnt vmcnt(12)
	v_cndmask_b32_e32 v19, 0, v55, vcc
	v_cndmask_b32_e32 v21, 0, v54, vcc
	s_cselect_b64 vcc, -1, 0
	s_cmp_gt_i32 s36, 33
	s_waitcnt vmcnt(11)
	v_cndmask_b32_e64 v23, 0, v53, s[4:5]
	s_waitcnt vmcnt(10)
	v_add_u32_e32 v27, v58, v54
	v_cndmask_b32_e32 v32, 0, v59, vcc
	v_cndmask_b32_e32 v34, 0, v58, vcc
	v_add_co_u32_e32 v54, vcc, s3, v50
	v_add_u32_e32 v29, v59, v55
	s_nop 0
	v_addc_co_u32_e32 v55, vcc, 0, v51, vcc
	s_mov_b32 s3, 0xc000
	v_add_co_u32_e32 v58, vcc, s3, v50
	v_cndmask_b32_e64 v25, 0, v52, s[4:5]
	s_cselect_b64 s[4:5], -1, 0
	v_addc_co_u32_e32 v59, vcc, 0, v51, vcc
	s_cmp_gt_i32 s36, 55
	global_load_dwordx2 v[58:59], v[58:59], off offset:3456
	s_cselect_b64 vcc, -1, 0
	global_load_dwordx2 v[54:55], v[54:55], off offset:3744
	s_waitcnt vmcnt(11)
	v_cndmask_b32_e64 v31, 0, v57, s[4:5]
	s_waitcnt vmcnt(10)
	v_cndmask_b32_e32 v40, 0, v63, vcc
	s_mov_b32 s3, 0xe000
	v_add_u32_e32 v21, v34, v21
	v_add3_u32 v34, v56, v52, v62
	v_add3_u32 v23, v31, v23, v40
	v_cndmask_b32_e32 v40, 0, v62, vcc
	v_add_co_u32_e32 v52, vcc, s3, v50
	v_add3_u32 v36, v57, v53, v63
	s_nop 0
	v_addc_co_u32_e32 v53, vcc, 0, v51, vcc
	global_load_dwordx2 v[52:53], v[52:53], off offset:4032
	s_cmp_gt_i32 s36, 44
	v_add_u32_e32 v19, v32, v19
	v_cndmask_b32_e64 v32, 0, v56, s[4:5]
	s_cselect_b64 s[4:5], -1, 0
	s_cmpk_gt_i32 s36, 0x42
	s_cselect_b64 vcc, -1, 0
	s_cmpk_gt_i32 s36, 0x4d
	s_waitcnt vmcnt(10)
	v_cndmask_b32_e64 v38, 0, v61, s[4:5]
	v_cndmask_b32_e64 v31, 0, v60, s[4:5]
	v_add3_u32 v25, v32, v25, v40
	s_cselect_b64 s[4:5], -1, 0
	s_waitcnt vmcnt(9)
	v_cndmask_b32_e32 v40, 0, v67, vcc
	s_cmp_gt_i32 s36, 12
	v_add3_u32 v19, v38, v19, v40
	v_cndmask_b32_e32 v40, 0, v66, vcc
	s_cselect_b64 vcc, -1, 0
	s_waitcnt vmcnt(8)
	v_cndmask_b32_e64 v32, 0, v69, s[4:5]
	v_add3_u32 v21, v31, v21, v40
	s_waitcnt vmcnt(7)
	v_cndmask_b32_e32 v40, 0, v71, vcc
	s_mov_b32 s3, 0x10000
	s_cmp_gt_i32 s36, 1
	v_add3_u32 v23, v32, v23, v40
	v_cndmask_b32_e32 v40, 0, v70, vcc
	v_add_co_u32_e32 v56, vcc, s3, v50
	v_cndmask_b32_e64 v38, 0, v68, s[4:5]
	s_cselect_b64 s[4:5], -1, 0
	v_addc_co_u32_e32 v57, vcc, 0, v51, vcc
	s_cmp_gt_i32 s36, 23
	s_cselect_b64 vcc, -1, 0
	v_add3_u32 v31, v68, v34, v70
	v_add3_u32 v34, v69, v36, v71
	s_waitcnt vmcnt(6)
	v_cndmask_b32_e64 v36, 0, v73, s[4:5]
	v_add3_u32 v25, v38, v25, v40
	s_waitcnt vmcnt(5)
	v_cndmask_b32_e32 v40, 0, v75, vcc
	s_mov_b32 s3, 0x12000
	v_add3_u32 v27, v60, v27, v66
	v_add3_u32 v19, v36, v19, v40
	v_cndmask_b32_e32 v40, 0, v74, vcc
	v_add_co_u32_e32 v60, vcc, s3, v50
	v_add3_u32 v29, v61, v29, v67
	s_nop 0
	v_addc_co_u32_e32 v61, vcc, 0, v51, vcc
	global_load_dwordx2 v[56:57], v[56:57], off offset:224
	s_mov_b32 s3, 0x11000
	global_load_dwordx2 v[60:61], v[60:61], off offset:800
	s_cmp_gt_i32 s36, 34
	v_add_co_u32_e32 v62, vcc, s3, v50
	v_cndmask_b32_e64 v32, 0, v72, s[4:5]
	s_cselect_b64 s[4:5], -1, 0
	v_addc_co_u32_e32 v63, vcc, 0, v51, vcc
	s_cmp_gt_i32 s36, 56
	s_cselect_b64 vcc, -1, 0
	s_waitcnt vmcnt(6)
	v_cndmask_b32_e64 v38, 0, v77, s[4:5]
	v_add3_u32 v21, v32, v21, v40
	s_mov_b32 s3, 0x13000
	s_cmp_gt_i32 s36, 45
	v_add3_u32 v27, v72, v27, v74
	v_cndmask_b32_e64 v36, 0, v76, s[4:5]
	s_cselect_b64 s[4:5], -1, 0
	v_add3_u32 v29, v73, v29, v75
	global_load_dwordx2 v[62:63], v[62:63], off offset:512
	s_waitcnt vmcnt(4)
	v_cndmask_b32_e32 v40, 0, v55, vcc
	v_add3_u32 v31, v76, v31, v54
	v_add3_u32 v23, v38, v23, v40
	v_cndmask_b32_e32 v40, 0, v54, vcc
	v_add_co_u32_e32 v54, vcc, s3, v50
	v_add3_u32 v32, v77, v34, v55
	s_nop 0
	v_addc_co_u32_e32 v55, vcc, 0, v51, vcc
	s_mov_b32 s3, 0x14000
	v_add_co_u32_e32 v66, vcc, s3, v50
	s_mov_b32 s3, 0x16000
	v_cndmask_b32_e64 v34, 0, v59, s[4:5]
	v_cndmask_b32_e64 v38, 0, v58, s[4:5]
	s_waitcnt vmcnt(3)
	v_add3_u32 v27, v58, v27, v52
	v_add_co_u32_e64 v58, s[4:5], s3, v50
	v_add3_u32 v29, v59, v29, v53
	s_nop 0
	v_addc_co_u32_e64 v59, s[4:5], 0, v51, s[4:5]
	global_load_dwordx2 v[58:59], v[58:59], off offset:1952
	s_mov_b32 s3, 0x15000
	global_load_dwordx2 v[54:55], v[54:55], off offset:1088
	v_add_co_u32_e64 v68, s[4:5], s3, v50
	v_addc_co_u32_e32 v67, vcc, 0, v51, vcc
	s_nop 0
	v_addc_co_u32_e64 v69, s[4:5], 0, v51, s[4:5]
	s_mov_b32 s3, 0x17000
	global_load_dwordx2 v[66:67], v[66:67], off offset:1376
	v_add_co_u32_e64 v70, s[4:5], s3, v50
	s_cmpk_gt_i32 s36, 0x43
	s_nop 0
	v_addc_co_u32_e64 v71, s[4:5], 0, v51, s[4:5]
	s_cselect_b64 vcc, -1, 0
	global_load_dwordx2 v[68:69], v[68:69], off offset:1664
	s_mov_b32 s3, 0x18000
	global_load_dwordx2 v[70:71], v[70:71], off offset:2240
	v_add3_u32 v25, v36, v25, v40
	v_add_co_u32_e64 v72, s[4:5], s3, v50
	v_cndmask_b32_e32 v40, 0, v53, vcc
	s_mov_b32 s3, 0x1a000
	v_add3_u32 v19, v34, v19, v40
	v_cndmask_b32_e32 v40, 0, v52, vcc
	v_add_co_u32_e32 v52, vcc, s3, v50
	v_addc_co_u32_e64 v73, s[4:5], 0, v51, s[4:5]
	s_nop 0
	v_addc_co_u32_e32 v53, vcc, 0, v51, vcc
	s_mov_b32 s3, 0x19000
	s_cmpk_gt_i32 s36, 0x4e
	global_load_dwordx2 v[72:73], v[72:73], off offset:2528
	v_add_co_u32_e32 v74, vcc, s3, v50
	global_load_dwordx2 v[52:53], v[52:53], off offset:3104
	s_cselect_b64 s[4:5], -1, 0
	v_addc_co_u32_e32 v75, vcc, 0, v51, vcc
	s_cmp_gt_i32 s36, 13
	s_cselect_b64 vcc, -1, 0
	s_waitcnt vmcnt(9)
	v_cndmask_b32_e64 v36, 0, v57, s[4:5]
	v_add3_u32 v21, v38, v21, v40
	s_waitcnt vmcnt(8)
	v_cndmask_b32_e32 v40, 0, v61, vcc
	s_mov_b32 s3, 0x1b000
	v_cndmask_b32_e64 v34, 0, v56, s[4:5]
	v_add3_u32 v31, v56, v31, v60
	v_add3_u32 v23, v36, v23, v40
	v_cndmask_b32_e32 v40, 0, v60, vcc
	v_add_co_u32_e32 v56, vcc, s3, v50
	v_add3_u32 v32, v57, v32, v61
	s_nop 0
	v_addc_co_u32_e32 v57, vcc, 0, v51, vcc
	global_load_dwordx2 v[74:75], v[74:75], off offset:2816
	s_mov_b32 s3, 0x1c000
	global_load_dwordx2 v[56:57], v[56:57], off offset:3392
	s_cmp_gt_i32 s36, 2
	v_add_co_u32_e32 v60, vcc, s3, v50
	s_cselect_b64 s[4:5], -1, 0
	s_nop 0
	v_addc_co_u32_e32 v61, vcc, 0, v51, vcc
	s_cmp_gt_i32 s36, 24
	s_cselect_b64 vcc, -1, 0
	s_waitcnt vmcnt(9)
	v_cndmask_b32_e64 v38, 0, v63, s[4:5]
	v_add3_u32 v25, v34, v25, v40
	s_mov_b32 s3, 0x1f000
	s_cmp_gt_i32 s36, 35
	v_cndmask_b32_e64 v36, 0, v62, s[4:5]
	s_cselect_b64 s[4:5], -1, 0
	s_cmp_gt_i32 s36, 57
	global_load_dwordx2 v[60:61], v[60:61], off offset:3680
	s_waitcnt vmcnt(8)
	v_cndmask_b32_e32 v40, 0, v55, vcc
	v_add3_u32 v27, v62, v27, v54
	v_add3_u32 v19, v38, v19, v40
	v_cndmask_b32_e32 v40, 0, v54, vcc
	v_add_co_u32_e32 v54, vcc, s3, v50
	v_add3_u32 v29, v63, v29, v55
	s_nop 0
	v_addc_co_u32_e32 v55, vcc, 0, v51, vcc
	s_cselect_b64 vcc, -1, 0
	s_cmp_gt_i32 s36, 46
	s_waitcnt vmcnt(7)
	v_cndmask_b32_e64 v34, 0, v67, s[4:5]
	v_cndmask_b32_e64 v38, 0, v66, s[4:5]
	v_add3_u32 v21, v36, v21, v40
	s_cselect_b64 s[4:5], -1, 0
	v_cndmask_b32_e32 v40, 0, v59, vcc
	s_cmpk_gt_i32 s36, 0x44
	v_add3_u32 v23, v34, v23, v40
	v_cndmask_b32_e32 v40, 0, v58, vcc
	s_cselect_b64 vcc, -1, 0
	s_waitcnt vmcnt(6)
	v_cndmask_b32_e64 v36, 0, v69, s[4:5]
	v_add3_u32 v25, v38, v25, v40
	s_waitcnt vmcnt(5)
	v_cndmask_b32_e32 v40, 0, v71, vcc
	s_mov_b32 s3, 0x1d000
	global_load_dwordx2 v[54:55], v[54:55], off offset:160
	v_add3_u32 v31, v66, v31, v58
	s_cmpk_gt_i32 s36, 0x4f
	v_add3_u32 v19, v36, v19, v40
	v_cndmask_b32_e32 v40, 0, v70, vcc
	v_add_co_u32_e32 v58, vcc, s3, v50
	v_add3_u32 v32, v67, v32, v59
	v_cndmask_b32_e64 v34, 0, v68, s[4:5]
	s_cselect_b64 s[4:5], -1, 0
	v_addc_co_u32_e32 v59, vcc, 0, v51, vcc
	s_cmp_gt_i32 s36, 14
	s_cselect_b64 vcc, -1, 0
	s_waitcnt vmcnt(5)
	v_cndmask_b32_e64 v38, 0, v73, s[4:5]
	v_add3_u32 v21, v34, v21, v40
	s_waitcnt vmcnt(4)
	v_cndmask_b32_e32 v40, 0, v53, vcc
	s_mov_b32 s3, 0x20000
	v_add3_u32 v31, v72, v31, v52
	v_add3_u32 v23, v38, v23, v40
	v_cndmask_b32_e32 v40, 0, v52, vcc
	v_add_co_u32_e32 v52, vcc, s3, v50
	v_add3_u32 v32, v73, v32, v53
	s_nop 0
	v_addc_co_u32_e32 v53, vcc, 0, v51, vcc
	s_mov_b32 s3, 0x21000
	s_cmp_gt_i32 s36, 3
	v_add_co_u32_e32 v62, vcc, s3, v50
	v_cndmask_b32_e64 v36, 0, v72, s[4:5]
	s_cselect_b64 s[4:5], -1, 0
	v_addc_co_u32_e32 v63, vcc, 0, v51, vcc
	s_cmp_gt_i32 s36, 25
	s_cselect_b64 vcc, -1, 0
	v_add3_u32 v27, v68, v27, v70
	s_waitcnt vmcnt(3)
	v_cndmask_b32_e64 v34, 0, v75, s[4:5]
	v_add3_u32 v25, v36, v25, v40
	s_waitcnt vmcnt(2)
	v_cndmask_b32_e32 v40, 0, v57, vcc
	s_mov_b32 s3, 0x23000
	v_add3_u32 v29, v69, v29, v71
	v_add3_u32 v27, v74, v27, v56
	v_add3_u32 v19, v34, v19, v40
	v_cndmask_b32_e32 v40, 0, v56, vcc
	v_add_co_u32_e32 v56, vcc, s3, v50
	v_add3_u32 v29, v75, v29, v57
	s_nop 0
	v_addc_co_u32_e32 v57, vcc, 0, v51, vcc
	global_load_dwordx2 v[58:59], v[58:59], off offset:3968
	s_cmp_gt_i32 s36, 36
	global_load_dwordx2 v[56:57], v[56:57], off offset:1312
	s_mov_b32 s3, 0x22000
	global_load_dwordx2 v[52:53], v[52:53], off offset:448
	v_cndmask_b32_e64 v38, 0, v74, s[4:5]
	global_load_dwordx2 v[62:63], v[62:63], off offset:736
	s_cselect_b64 s[4:5], -1, 0
	v_add_co_u32_e32 v66, vcc, s3, v50
	s_mov_b32 s3, 0x24000
	s_waitcnt vmcnt(5)
	v_cndmask_b32_e64 v36, 0, v61, s[4:5]
	v_cndmask_b32_e64 v34, 0, v60, s[4:5]
	v_addc_co_u32_e32 v67, vcc, 0, v51, vcc
	s_cmp_gt_i32 s36, 58
	s_cselect_b64 vcc, -1, 0
	v_add3_u32 v21, v38, v21, v40
	global_load_dwordx2 v[66:67], v[66:67], off offset:1024
	s_cmp_gt_i32 s36, 47
	s_waitcnt vmcnt(5)
	v_add3_u32 v31, v60, v31, v54
	v_add_co_u32_e64 v60, s[4:5], s3, v50
	v_add3_u32 v32, v61, v32, v55
	s_nop 0
	v_addc_co_u32_e64 v61, s[4:5], 0, v51, s[4:5]
	s_mov_b32 s3, 0x25000
	v_add_co_u32_e64 v68, s[4:5], s3, v50
	s_mov_b32 s3, 0x27000
	s_nop 0
	v_addc_co_u32_e64 v69, s[4:5], 0, v51, s[4:5]
	v_add_co_u32_e64 v70, s[4:5], s3, v50
	s_mov_b32 s3, 0x26000
	s_nop 0
	v_addc_co_u32_e64 v71, s[4:5], 0, v51, s[4:5]
	v_add_co_u32_e64 v72, s[4:5], s3, v50
	v_cndmask_b32_e32 v40, 0, v55, vcc
	s_mov_b32 s3, 0x28000
	v_add3_u32 v23, v36, v23, v40
	v_cndmask_b32_e32 v40, 0, v54, vcc
	v_add_co_u32_e32 v54, vcc, s3, v50
	s_mov_b32 s3, 0x29000
	s_nop 0
	v_addc_co_u32_e32 v55, vcc, 0, v51, vcc
	global_load_dwordx2 v[68:69], v[68:69], off offset:1888
	v_addc_co_u32_e64 v73, s[4:5], 0, v51, s[4:5]
	global_load_dwordx2 v[60:61], v[60:61], off offset:1600
	v_add_co_u32_e32 v74, vcc, s3, v50
	s_cselect_b64 s[4:5], -1, 0
	s_nop 0
	v_addc_co_u32_e32 v75, vcc, 0, v51, vcc
	s_cmpk_gt_i32 s36, 0x45
	global_load_dwordx2 v[70:71], v[70:71], off offset:2464
	s_cselect_b64 vcc, -1, 0
	v_add3_u32 v25, v34, v25, v40
	s_mov_b32 s3, 0x2b000
	global_load_dwordx2 v[72:73], v[72:73], off offset:2176
	s_cmpk_gt_i32 s36, 0x50
	global_load_dwordx2 v[54:55], v[54:55], off offset:2752
	s_waitcnt vmcnt(9)
	v_cndmask_b32_e64 v38, 0, v59, s[4:5]
	v_cndmask_b32_e64 v36, 0, v58, s[4:5]
	s_cselect_b64 s[4:5], -1, 0
	s_cmp_gt_i32 s36, 15
	s_waitcnt vmcnt(7)
	v_cndmask_b32_e32 v40, 0, v53, vcc
	v_add3_u32 v27, v58, v27, v52
	v_add3_u32 v19, v38, v19, v40
	v_cndmask_b32_e32 v40, 0, v52, vcc
	v_add_co_u32_e32 v52, vcc, s3, v50
	v_add3_u32 v29, v59, v29, v53
	s_nop 0
	v_addc_co_u32_e32 v53, vcc, 0, v51, vcc
	s_mov_b32 s3, 0x2a000
	v_add_co_u32_e32 v58, vcc, s3, v50
	s_waitcnt vmcnt(6)
	v_cndmask_b32_e64 v34, 0, v63, s[4:5]
	v_addc_co_u32_e32 v59, vcc, 0, v51, vcc
	s_cselect_b64 vcc, -1, 0
	v_add3_u32 v21, v36, v21, v40
	v_cndmask_b32_e32 v40, 0, v57, vcc
	s_mov_b32 s3, 0x2c000
	v_add3_u32 v31, v62, v31, v56
	v_add3_u32 v23, v34, v23, v40
	v_cndmask_b32_e32 v40, 0, v56, vcc
	v_add_co_u32_e32 v56, vcc, s3, v50
	v_add3_u32 v32, v63, v32, v57
	s_nop 0
	v_addc_co_u32_e32 v57, vcc, 0, v51, vcc
	global_load_dwordx2 v[74:75], v[74:75], off offset:3040
	s_cmp_gt_i32 s36, 4
	global_load_dwordx2 v[58:59], v[58:59], off offset:3328
	v_cndmask_b32_e64 v38, 0, v62, s[4:5]
	global_load_dwordx2 v[56:57], v[56:57], off offset:3904
	s_cselect_b64 s[4:5], -1, 0
	global_load_dwordx2 v[52:53], v[52:53], off offset:3616
	s_cmp_gt_i32 s36, 26
	s_cselect_b64 vcc, -1, 0
	s_cmp_gt_i32 s36, 37
	s_waitcnt vmcnt(9)
	v_cndmask_b32_e64 v36, 0, v67, s[4:5]
	v_cndmask_b32_e64 v34, 0, v66, s[4:5]
	v_add3_u32 v25, v38, v25, v40
	s_cselect_b64 s[4:5], -1, 0
	s_cmp_gt_i32 s36, 59
	s_mov_b32 s3, 0x2e000
	s_waitcnt vmcnt(8)
	v_cndmask_b32_e64 v38, 0, v69, s[4:5]
	s_waitcnt vmcnt(7)
	v_cndmask_b32_e32 v40, 0, v61, vcc
	v_add3_u32 v19, v36, v19, v40
	v_cndmask_b32_e32 v40, 0, v60, vcc
	s_cselect_b64 vcc, -1, 0
	v_add3_u32 v21, v34, v21, v40
	v_add3_u32 v27, v66, v27, v60
	s_cmp_gt_i32 s36, 48
	s_waitcnt vmcnt(6)
	v_cndmask_b32_e32 v40, 0, v71, vcc
	v_add3_u32 v23, v38, v23, v40
	v_cndmask_b32_e32 v40, 0, v70, vcc
	v_add_co_u32_e32 v60, vcc, s3, v50
	v_add3_u32 v29, v67, v29, v61
	v_cndmask_b32_e64 v36, 0, v68, s[4:5]
	s_cselect_b64 s[4:5], -1, 0
	v_addc_co_u32_e32 v61, vcc, 0, v51, vcc
	s_cmpk_gt_i32 s36, 0x46
	s_cselect_b64 vcc, -1, 0
	s_waitcnt vmcnt(5)
	v_cndmask_b32_e64 v34, 0, v73, s[4:5]
	v_add3_u32 v25, v36, v25, v40
	s_waitcnt vmcnt(4)
	v_cndmask_b32_e32 v40, 0, v55, vcc
	s_mov_b32 s3, 0x30000
	v_add3_u32 v27, v72, v27, v54
	v_add3_u32 v19, v34, v19, v40
	v_cndmask_b32_e32 v40, 0, v54, vcc
	v_add_co_u32_e32 v54, vcc, s3, v50
	v_add3_u32 v29, v73, v29, v55
	s_nop 0
	v_addc_co_u32_e32 v55, vcc, 0, v51, vcc
	s_mov_b32 s3, 0x2f000
	s_cmpk_gt_i32 s36, 0x51
	v_add_co_u32_e32 v62, vcc, s3, v50
	v_cndmask_b32_e64 v38, 0, v72, s[4:5]
	s_cselect_b64 s[4:5], -1, 0
	v_addc_co_u32_e32 v63, vcc, 0, v51, vcc
	s_cmp_gt_i32 s36, 16
	s_cselect_b64 vcc, -1, 0
	v_add3_u32 v31, v68, v31, v70
	v_add3_u32 v21, v38, v21, v40
	s_mov_b32 s3, 0x31000
	v_add3_u32 v32, v69, v32, v71
	s_cmp_gt_i32 s36, 5
	global_load_dwordx2 v[60:61], v[60:61], off offset:96
	s_waitcnt vmcnt(4)
	v_cndmask_b32_e64 v36, 0, v75, s[4:5]
	v_cndmask_b32_e64 v34, 0, v74, s[4:5]
	global_load_dwordx2 v[54:55], v[54:55], off offset:672
	s_cselect_b64 s[4:5], -1, 0
	s_waitcnt vmcnt(4)
	v_cndmask_b32_e64 v38, 0, v59, s[4:5]
	s_waitcnt vmcnt(3)
	v_add3_u32 v27, v58, v27, v56
	s_waitcnt vmcnt(2)
	v_cndmask_b32_e32 v40, 0, v53, vcc
	v_add3_u32 v31, v74, v31, v52
	v_add3_u32 v23, v36, v23, v40
	v_cndmask_b32_e32 v40, 0, v52, vcc
	v_add_co_u32_e32 v52, vcc, s3, v50
	v_add3_u32 v32, v75, v32, v53
	s_nop 0
	v_addc_co_u32_e32 v53, vcc, 0, v51, vcc
	s_mov_b32 s3, 0x32000
	v_add_co_u32_e32 v66, vcc, s3, v50
	s_mov_b32 s3, 0x34000
	v_cndmask_b32_e64 v36, 0, v58, s[4:5]
	v_add_co_u32_e64 v58, s[4:5], s3, v50
	v_add3_u32 v29, v59, v29, v57
	s_nop 0
	v_addc_co_u32_e64 v59, s[4:5], 0, v51, s[4:5]
	s_mov_b32 s3, 0x33000
	v_add_co_u32_e64 v68, s[4:5], s3, v50
	s_mov_b32 s3, 0x35000
	s_nop 0
	v_addc_co_u32_e64 v69, s[4:5], 0, v51, s[4:5]
	v_addc_co_u32_e32 v67, vcc, 0, v51, vcc
	s_cmp_gt_i32 s36, 27
	v_add_co_u32_e64 v70, s[4:5], s3, v50
	s_cselect_b64 vcc, -1, 0
	s_nop 0
	v_addc_co_u32_e64 v71, s[4:5], 0, v51, s[4:5]
	s_mov_b32 s3, 0x36000
	v_add3_u32 v25, v34, v25, v40
	v_add_co_u32_e64 v72, s[4:5], s3, v50
	v_cndmask_b32_e32 v40, 0, v57, vcc
	s_mov_b32 s3, 0x38000
	v_add3_u32 v19, v38, v19, v40
	v_cndmask_b32_e32 v40, 0, v56, vcc
	v_add_co_u32_e32 v56, vcc, s3, v50
	global_load_dwordx2 v[62:63], v[62:63], off offset:384
	s_nop 0
	v_addc_co_u32_e32 v57, vcc, 0, v51, vcc
	global_load_dwordx2 v[58:59], v[58:59], off offset:1824
	v_addc_co_u32_e64 v73, s[4:5], 0, v51, s[4:5]
	global_load_dwordx2 v[56:57], v[56:57], off offset:2976
	s_cmp_gt_i32 s36, 38
	global_load_dwordx2 v[52:53], v[52:53], off offset:960
	s_mov_b32 s3, 0x37000
	global_load_dwordx2 v[66:67], v[66:67], off offset:1248
	s_cselect_b64 s[4:5], -1, 0
	global_load_dwordx2 v[68:69], v[68:69], off offset:1536
	v_add_co_u32_e32 v74, vcc, s3, v50
	global_load_dwordx2 v[70:71], v[70:71], off offset:2112
	s_mov_b32 s3, 0x39000
	global_load_dwordx2 v[72:73], v[72:73], off offset:2400
	v_addc_co_u32_e32 v75, vcc, 0, v51, vcc
	global_load_dwordx2 v[74:75], v[74:75], off offset:2688
	s_cmp_gt_i32 s36, 60
	s_cselect_b64 vcc, -1, 0
	s_cmp_gt_i32 s36, 49
	v_add3_u32 v21, v36, v21, v40
	s_waitcnt vmcnt(10)
	v_cndmask_b32_e64 v34, 0, v61, s[4:5]
	v_cndmask_b32_e64 v38, 0, v60, s[4:5]
	s_waitcnt vmcnt(9)
	v_add3_u32 v31, v60, v31, v54
	v_add_co_u32_e64 v60, s[4:5], s3, v50
	v_add3_u32 v32, v61, v32, v55
	s_nop 0
	v_addc_co_u32_e64 v61, s[4:5], 0, v51, s[4:5]
	global_load_dwordx2 v[60:61], v[60:61], off offset:3264
	s_mov_b32 s3, 0x3a000
	v_add_co_u32_e64 v76, s[4:5], s3, v50
	v_cndmask_b32_e32 v40, 0, v55, vcc
	s_nop 0
	v_addc_co_u32_e64 v77, s[4:5], 0, v51, s[4:5]
	global_load_dwordx2 v[76:77], v[76:77], off offset:3552
	s_cselect_b64 s[4:5], -1, 0
	s_cmpk_gt_i32 s36, 0x47
	v_add3_u32 v23, v34, v23, v40
	v_cndmask_b32_e32 v40, 0, v54, vcc
	s_cselect_b64 vcc, -1, 0
	v_add3_u32 v25, v38, v25, v40
	s_mov_b32 s3, 0x3d000
	s_cmpk_gt_i32 s36, 0x52
	s_waitcnt vmcnt(10)
	v_cndmask_b32_e64 v36, 0, v63, s[4:5]
	v_cndmask_b32_e64 v34, 0, v62, s[4:5]
	s_cselect_b64 s[4:5], -1, 0
	s_cmp_gt_i32 s36, 17
	s_waitcnt vmcnt(7)
	v_cndmask_b32_e32 v40, 0, v53, vcc
	v_add3_u32 v27, v62, v27, v52
	v_add3_u32 v19, v36, v19, v40
	v_cndmask_b32_e32 v40, 0, v52, vcc
	v_add_co_u32_e32 v52, vcc, s3, v50
	v_add3_u32 v29, v63, v29, v53
	s_nop 0
	v_addc_co_u32_e32 v53, vcc, 0, v51, vcc
	s_cselect_b64 vcc, -1, 0
	s_cmp_gt_i32 s36, 6
	s_waitcnt vmcnt(6)
	v_cndmask_b32_e64 v38, 0, v67, s[4:5]
	v_cndmask_b32_e64 v36, 0, v66, s[4:5]
	v_add3_u32 v21, v34, v21, v40
	s_cselect_b64 s[4:5], -1, 0
	v_cndmask_b32_e32 v40, 0, v59, vcc
	s_cmp_gt_i32 s36, 28
	v_add3_u32 v23, v38, v23, v40
	v_cndmask_b32_e32 v40, 0, v58, vcc
	s_cselect_b64 vcc, -1, 0
	s_waitcnt vmcnt(5)
	v_cndmask_b32_e64 v34, 0, v69, s[4:5]
	v_add3_u32 v25, v36, v25, v40
	s_waitcnt vmcnt(4)
	v_cndmask_b32_e32 v40, 0, v71, vcc
	s_mov_b32 s3, 0x3b000
	s_cmp_gt_i32 s36, 39
	v_add3_u32 v19, v34, v19, v40
	v_cndmask_b32_e32 v40, 0, v70, vcc
	v_add_co_u32_e32 v54, vcc, s3, v50
	global_load_dwordx2 v[52:53], v[52:53], off offset:32
	v_cndmask_b32_e64 v38, 0, v68, s[4:5]
	s_cselect_b64 s[4:5], -1, 0
	v_addc_co_u32_e32 v55, vcc, 0, v51, vcc
	s_cmp_gt_i32 s36, 61
	s_cselect_b64 vcc, -1, 0
	v_add3_u32 v31, v66, v31, v58
	s_waitcnt vmcnt(4)
	v_cndmask_b32_e64 v36, 0, v73, s[4:5]
	v_add3_u32 v21, v38, v21, v40
	v_cndmask_b32_e32 v40, 0, v57, vcc
	s_mov_b32 s3, 0x3e000
	v_add3_u32 v32, v67, v32, v59
	global_load_dwordx2 v[54:55], v[54:55], off offset:3840
	v_add3_u32 v31, v72, v31, v56
	v_add3_u32 v23, v36, v23, v40
	v_cndmask_b32_e32 v40, 0, v56, vcc
	v_add_co_u32_e32 v56, vcc, s3, v50
	v_add3_u32 v32, v73, v32, v57
	s_nop 0
	v_addc_co_u32_e32 v57, vcc, 0, v51, vcc
	global_load_dwordx2 v[56:57], v[56:57], off offset:320
	s_cmp_gt_i32 s36, 50
	v_cndmask_b32_e64 v34, 0, v72, s[4:5]
	s_cselect_b64 s[4:5], -1, 0
	s_cmpk_gt_i32 s36, 0x48
	s_cselect_b64 vcc, -1, 0
	s_waitcnt vmcnt(5)
	v_cndmask_b32_e64 v38, 0, v75, s[4:5]
	v_add3_u32 v25, v34, v25, v40
	s_waitcnt vmcnt(4)
	v_cndmask_b32_e32 v40, 0, v61, vcc
	s_mov_b32 s3, 0x3f000
	v_add3_u32 v19, v38, v19, v40
	v_cndmask_b32_e32 v40, 0, v60, vcc
	v_add_co_u32_e32 v58, vcc, s3, v50
	v_add3_u32 v27, v68, v27, v70
	s_nop 0
	v_addc_co_u32_e32 v59, vcc, 0, v51, vcc
	s_mov_b32 s3, 0x40000
	v_add3_u32 v29, v69, v29, v71
	v_add3_u32 v27, v74, v27, v60
	v_add_co_u32_e32 v60, vcc, s3, v50
	v_add3_u32 v29, v75, v29, v61
	s_cmpk_gt_i32 s36, 0x53
	v_addc_co_u32_e32 v61, vcc, 0, v51, vcc
	s_mov_b32 s3, 0x41000
	v_cndmask_b32_e64 v36, 0, v74, s[4:5]
	s_cselect_b64 s[4:5], -1, 0
	v_add_co_u32_e32 v62, vcc, s3, v50
	s_mov_b32 s3, 0x42000
	s_waitcnt vmcnt(3)
	v_cndmask_b32_e64 v34, 0, v77, s[4:5]
	v_cndmask_b32_e64 v38, 0, v76, s[4:5]
	v_add_co_u32_e64 v66, s[4:5], s3, v50
	s_mov_b32 s3, 0x43000
	s_nop 0
	v_addc_co_u32_e64 v67, s[4:5], 0, v51, s[4:5]
	v_add_co_u32_e64 v68, s[4:5], s3, v50
	s_mov_b32 s3, 0x45000
	s_nop 0
	v_addc_co_u32_e64 v69, s[4:5], 0, v51, s[4:5]
	global_load_dwordx2 v[58:59], v[58:59], off offset:608
	v_addc_co_u32_e32 v63, vcc, 0, v51, vcc
	v_add_co_u32_e64 v70, s[4:5], s3, v50
	global_load_dwordx2 v[62:63], v[62:63], off offset:1184
	s_nop 0
	global_load_dwordx2 v[60:61], v[60:61], off offset:896
	v_addc_co_u32_e64 v71, s[4:5], 0, v51, s[4:5]
	s_mov_b32 s3, 0x44000
	global_load_dwordx2 v[66:67], v[66:67], off offset:1472
	v_add_co_u32_e64 v72, s[4:5], s3, v50
	s_mov_b32 s3, 0x46000
	s_nop 0
	v_addc_co_u32_e64 v73, s[4:5], 0, v51, s[4:5]
	global_load_dwordx2 v[68:69], v[68:69], off offset:1760
	v_add_co_u32_e64 v74, s[4:5], s3, v50
	global_load_dwordx2 v[70:71], v[70:71], off offset:2336
	s_nop 0
	v_addc_co_u32_e64 v75, s[4:5], 0, v51, s[4:5]
	s_mov_b32 s3, 0x47000
	s_waitcnt vmcnt(8)
	v_add3_u32 v31, v76, v31, v52
	s_cmp_gt_i32 s36, 18
	global_load_dwordx2 v[72:73], v[72:73], off offset:2048
	v_add_co_u32_e64 v76, s[4:5], s3, v50
	global_load_dwordx2 v[74:75], v[74:75], off offset:2624
	v_add3_u32 v32, v77, v32, v53
	s_cselect_b64 vcc, -1, 0
	s_cmp_gt_i32 s36, 7
	v_addc_co_u32_e64 v77, s[4:5], 0, v51, s[4:5]
	v_add3_u32 v21, v36, v21, v40
	s_cselect_b64 s[4:5], -1, 0
	v_cndmask_b32_e32 v40, 0, v53, vcc
	s_mov_b32 s3, 0x49000
	s_waitcnt vmcnt(9)
	v_cndmask_b32_e64 v36, 0, v55, s[4:5]
	v_add3_u32 v23, v34, v23, v40
	v_cndmask_b32_e64 v34, 0, v54, s[4:5]
	v_cndmask_b32_e32 v40, 0, v52, vcc
	s_cmp_gt_i32 s36, 29
	v_add_co_u32_e64 v52, s[4:5], s3, v50
	s_cselect_b64 vcc, -1, 0
	s_nop 0
	v_addc_co_u32_e64 v53, s[4:5], 0, v51, s[4:5]
	s_mov_b32 s3, 0x48000
	v_add3_u32 v25, v38, v25, v40
	s_waitcnt vmcnt(8)
	v_add3_u32 v27, v54, v27, v56
	v_add_co_u32_e64 v54, s[4:5], s3, v50
	v_cndmask_b32_e32 v40, 0, v57, vcc
	s_mov_b32 s3, 0x4a000
	global_load_dwordx2 v[76:77], v[76:77], off offset:2912
	v_add3_u32 v19, v36, v19, v40
	global_load_dwordx2 v[52:53], v[52:53], off offset:3488
	v_cndmask_b32_e32 v40, 0, v56, vcc
	v_add_co_u32_e32 v56, vcc, s3, v50
	v_add3_u32 v29, v55, v29, v57
	v_addc_co_u32_e64 v55, s[4:5], 0, v51, s[4:5]
	v_addc_co_u32_e32 v57, vcc, 0, v51, vcc
	global_load_dwordx2 v[54:55], v[54:55], off offset:3200
	s_cmp_gt_i32 s36, 40
	global_load_dwordx2 v[56:57], v[56:57], off offset:3776
	s_cselect_b64 s[4:5], -1, 0
	s_cmp_gt_i32 s36, 62
	s_cselect_b64 vcc, -1, 0
	s_cmp_gt_i32 s36, 51
	v_add3_u32 v21, v34, v21, v40
	s_mov_b32 s3, 0x4b000
	s_waitcnt vmcnt(11)
	v_cndmask_b32_e64 v38, 0, v59, s[4:5]
	v_cndmask_b32_e64 v36, 0, v58, s[4:5]
	s_cselect_b64 s[4:5], -1, 0
	s_cmpk_gt_i32 s36, 0x49
	s_waitcnt vmcnt(10)
	v_cndmask_b32_e32 v40, 0, v63, vcc
	v_add3_u32 v23, v38, v23, v40
	v_cndmask_b32_e32 v40, 0, v62, vcc
	s_cselect_b64 vcc, -1, 0
	s_cmpk_gt_i32 s36, 0x54
	s_waitcnt vmcnt(9)
	v_cndmask_b32_e64 v34, 0, v61, s[4:5]
	v_cndmask_b32_e64 v38, 0, v60, s[4:5]
	v_add3_u32 v25, v36, v25, v40
	s_cselect_b64 s[4:5], -1, 0
	s_waitcnt vmcnt(8)
	v_cndmask_b32_e32 v40, 0, v67, vcc
	s_cmp_gt_i32 s36, 19
	v_add3_u32 v19, v34, v19, v40
	v_cndmask_b32_e32 v40, 0, v66, vcc
	s_cselect_b64 vcc, -1, 0
	s_cmp_gt_i32 s36, 8
	s_waitcnt vmcnt(7)
	v_cndmask_b32_e64 v36, 0, v69, s[4:5]
	v_cndmask_b32_e64 v34, 0, v68, s[4:5]
	v_add3_u32 v21, v38, v21, v40
	s_cselect_b64 s[4:5], -1, 0
	s_waitcnt vmcnt(6)
	v_cndmask_b32_e32 v40, 0, v71, vcc
	s_cmp_gt_i32 s36, 30
	v_add3_u32 v23, v36, v23, v40
	v_cndmask_b32_e32 v40, 0, v70, vcc
	s_cselect_b64 vcc, -1, 0
	s_waitcnt vmcnt(5)
	v_cndmask_b32_e64 v38, 0, v73, s[4:5]
	v_add3_u32 v25, v34, v25, v40
	s_waitcnt vmcnt(4)
	v_cndmask_b32_e32 v40, 0, v75, vcc
	v_add3_u32 v31, v58, v31, v62
	v_add3_u32 v19, v38, v19, v40
	v_cndmask_b32_e32 v40, 0, v74, vcc
	v_add_co_u32_e32 v58, vcc, s3, v50
	v_add3_u32 v32, v59, v32, v63
	s_nop 0
	v_addc_co_u32_e32 v59, vcc, 0, v51, vcc
	s_mov_b32 s3, 0x4d000
	v_add3_u32 v27, v60, v27, v66
	s_cmp_gt_i32 s36, 41
	v_add_co_u32_e32 v60, vcc, s3, v50
	v_add3_u32 v29, v61, v29, v67
	v_cndmask_b32_e64 v36, 0, v72, s[4:5]
	s_cselect_b64 s[4:5], -1, 0
	v_addc_co_u32_e32 v61, vcc, 0, v51, vcc
	s_cmp_gt_i32 s36, 63
	s_cselect_b64 vcc, -1, 0
	v_add3_u32 v31, v68, v31, v70
	v_add3_u32 v21, v36, v21, v40
	s_cmp_gt_i32 s36, 52
	s_waitcnt vmcnt(3)
	v_cndmask_b32_e64 v34, 0, v77, s[4:5]
	s_mov_b32 s3, 0x4e000
	s_waitcnt vmcnt(2)
	v_cndmask_b32_e32 v40, 0, v53, vcc
	v_add3_u32 v27, v72, v27, v74
	v_cndmask_b32_e64 v38, 0, v76, s[4:5]
	v_add3_u32 v31, v76, v31, v52
	s_cselect_b64 s[4:5], -1, 0
	v_add3_u32 v23, v34, v23, v40
	v_cndmask_b32_e32 v40, 0, v52, vcc
	v_add_co_u32_e32 v52, vcc, s3, v50
	s_mov_b32 s3, 0x4f000
	v_add3_u32 v29, v73, v29, v75
	s_waitcnt vmcnt(1)
	v_cndmask_b32_e64 v36, 0, v55, s[4:5]
	v_cndmask_b32_e64 v34, 0, v54, s[4:5]
	s_waitcnt vmcnt(0)
	v_add3_u32 v27, v54, v27, v56
	v_add_co_u32_e64 v54, s[4:5], s3, v50
	v_add3_u32 v29, v55, v29, v57
	s_nop 0
	v_addc_co_u32_e64 v55, s[4:5], 0, v51, s[4:5]
	s_mov_b32 s3, 0x50000
	v_add_co_u32_e64 v62, s[4:5], s3, v50
	s_mov_b32 s3, 0x52000
	s_nop 0
	v_addc_co_u32_e64 v63, s[4:5], 0, v51, s[4:5]
	v_add_co_u32_e64 v66, s[4:5], s3, v50
	s_mov_b32 s3, 0x51000
	s_nop 0
	v_addc_co_u32_e64 v67, s[4:5], 0, v51, s[4:5]
	v_add3_u32 v32, v69, v32, v71
	v_add_co_u32_e64 v68, s[4:5], s3, v50
	v_add3_u32 v32, v77, v32, v53
	v_addc_co_u32_e32 v53, vcc, 0, v51, vcc
	v_addc_co_u32_e64 v69, s[4:5], 0, v51, s[4:5]
	s_mov_b32 s3, 0x53000
	global_load_dwordx2 v[58:59], v[58:59], off offset:4064
	s_nop 0
	global_load_dwordx2 v[60:61], v[60:61], off offset:256
	v_add_co_u32_e64 v70, s[4:5], s3, v50
	global_load_dwordx2 v[52:53], v[52:53], off offset:544
	s_nop 0
	v_addc_co_u32_e64 v71, s[4:5], 0, v51, s[4:5]
	s_mov_b32 s3, 0x54000
	global_load_dwordx2 v[54:55], v[54:55], off offset:832
	v_add_co_u32_e64 v72, s[4:5], s3, v50
	s_mov_b32 s3, 0x56000
	s_nop 0
	v_addc_co_u32_e64 v73, s[4:5], 0, v51, s[4:5]
	global_load_dwordx2 v[62:63], v[62:63], off offset:1120
	v_add_co_u32_e64 v74, s[4:5], s3, v50
	global_load_dwordx2 v[66:67], v[66:67], off offset:1696
	s_nop 0
	v_addc_co_u32_e64 v75, s[4:5], 0, v51, s[4:5]
	s_mov_b32 s3, 0x55000
	global_load_dwordx2 v[68:69], v[68:69], off offset:1408
	v_add_co_u32_e64 v76, s[4:5], s3, v50
	global_load_dwordx2 v[70:71], v[70:71], off offset:1984
	s_nop 0
	v_addc_co_u32_e64 v77, s[4:5], 0, v51, s[4:5]
	s_mov_b32 s3, 0x57000
	global_load_dwordx2 v[72:73], v[72:73], off offset:2272
	v_add_co_u32_e64 v78, s[4:5], s3, v50
	global_load_dwordx2 v[74:75], v[74:75], off offset:2848
	s_cmpk_gt_i32 s36, 0x4a
	v_addc_co_u32_e64 v79, s[4:5], 0, v51, s[4:5]
	s_mov_b32 s3, 0x58000
	s_cselect_b64 vcc, -1, 0
	global_load_dwordx2 v[76:77], v[76:77], off offset:2560
	v_add_co_u32_e64 v80, s[4:5], s3, v50
	global_load_dwordx2 v[78:79], v[78:79], off offset:3136
	v_add3_u32 v25, v38, v25, v40
	v_addc_co_u32_e64 v81, s[4:5], 0, v51, s[4:5]
	v_cndmask_b32_e32 v40, 0, v57, vcc
	s_mov_b32 s3, 0x59000
	global_load_dwordx2 v[80:81], v[80:81], off offset:3424
	v_add3_u32 v19, v36, v19, v40
	v_cndmask_b32_e32 v40, 0, v56, vcc
	v_add_co_u32_e32 v50, vcc, s3, v50
	s_cmpk_gt_i32 s36, 0x55
	s_nop 0
	v_addc_co_u32_e32 v51, vcc, 0, v51, vcc
	global_load_dwordx2 v[56:57], v[50:51], off offset:3712
	s_cselect_b64 s[4:5], -1, 0
	s_cmp_gt_i32 s36, 20
	s_cselect_b64 vcc, -1, 0
	s_cmp_gt_i32 s36, 9
	v_add3_u32 v21, v34, v21, v40
	s_waitcnt vmcnt(13)
	v_cndmask_b32_e64 v38, 0, v59, s[4:5]
	v_cndmask_b32_e64 v36, 0, v58, s[4:5]
	s_cselect_b64 s[4:5], -1, 0
	s_cmp_gt_i32 s36, 31
	s_waitcnt vmcnt(11)
	v_cndmask_b32_e32 v40, 0, v53, vcc
	v_add3_u32 v23, v38, v23, v40
	v_cndmask_b32_e32 v40, 0, v52, vcc
	s_cselect_b64 vcc, -1, 0
	s_cmp_gt_i32 s36, 42
	v_cndmask_b32_e64 v34, 0, v61, s[4:5]
	v_cndmask_b32_e64 v38, 0, v60, s[4:5]
	v_add3_u32 v25, v36, v25, v40
	s_cselect_b64 s[4:5], -1, 0
	s_waitcnt vmcnt(10)
	v_cndmask_b32_e32 v40, 0, v55, vcc
	s_cmp_gt_i32 s36, 64
	v_add3_u32 v19, v34, v19, v40
	v_cndmask_b32_e32 v40, 0, v54, vcc
	s_cselect_b64 vcc, -1, 0
	s_cmp_gt_i32 s36, 53
	s_waitcnt vmcnt(9)
	v_cndmask_b32_e64 v36, 0, v63, s[4:5]
	v_cndmask_b32_e64 v34, 0, v62, s[4:5]
	v_add3_u32 v21, v38, v21, v40
	s_cselect_b64 s[4:5], -1, 0
	s_waitcnt vmcnt(8)
	v_cndmask_b32_e32 v40, 0, v67, vcc
	s_cmpk_gt_i32 s36, 0x4b
	v_add3_u32 v23, v36, v23, v40
	v_cndmask_b32_e32 v40, 0, v66, vcc
	s_cselect_b64 vcc, -1, 0
	s_cmpk_gt_i32 s36, 0x56
	s_waitcnt vmcnt(7)
	v_cndmask_b32_e64 v38, 0, v69, s[4:5]
	v_cndmask_b32_e64 v36, 0, v68, s[4:5]
	v_add3_u32 v25, v34, v25, v40
	s_cselect_b64 s[4:5], -1, 0
	s_waitcnt vmcnt(6)
	v_cndmask_b32_e32 v40, 0, v71, vcc
	s_cmp_gt_i32 s36, 21
	v_add3_u32 v19, v38, v19, v40
	v_cndmask_b32_e32 v40, 0, v70, vcc
	s_cselect_b64 vcc, -1, 0
	s_cmp_gt_i32 s36, 10
	s_waitcnt vmcnt(5)
	v_cndmask_b32_e64 v34, 0, v73, s[4:5]
	v_cndmask_b32_e64 v38, 0, v72, s[4:5]
	v_add3_u32 v21, v36, v21, v40
	s_cselect_b64 s[4:5], -1, 0
	s_waitcnt vmcnt(4)
	v_cndmask_b32_e32 v40, 0, v75, vcc
	s_cmp_gt_i32 s36, 32
	v_add3_u32 v23, v34, v23, v40
	v_cndmask_b32_e32 v40, 0, v74, vcc
	s_cselect_b64 vcc, -1, 0
	s_cmp_gt_i32 s36, 43
	s_waitcnt vmcnt(3)
	v_cndmask_b32_e64 v36, 0, v77, s[4:5]
	v_cndmask_b32_e64 v34, 0, v76, s[4:5]
	v_add3_u32 v25, v38, v25, v40
	s_cselect_b64 s[4:5], -1, 0
	s_waitcnt vmcnt(2)
	v_cndmask_b32_e32 v40, 0, v79, vcc
	s_cmpk_gt_i32 s36, 0x41
	v_add3_u32 v31, v58, v31, v52
	v_add3_u32 v32, v59, v32, v53
	v_add3_u32 v19, v36, v19, v40
	v_cndmask_b32_e32 v40, 0, v78, vcc
	s_cselect_b64 vcc, -1, 0
	v_add3_u32 v27, v60, v27, v54
	v_add3_u32 v29, v61, v29, v55
	v_add3_u32 v31, v62, v31, v66
	v_add3_u32 v32, v63, v32, v67
	s_waitcnt vmcnt(1)
	v_cndmask_b32_e64 v38, 0, v81, s[4:5]
	v_add3_u32 v21, v34, v21, v40
	s_cmp_gt_i32 s36, 54
	v_cndmask_b32_e32 v40, 0, v65, vcc
	v_add3_u32 v27, v68, v27, v70
	v_add3_u32 v29, v69, v29, v71
	v_add3_u32 v31, v72, v31, v74
	v_add3_u32 v32, v73, v32, v75
	v_cndmask_b32_e64 v36, 0, v80, s[4:5]
	s_cselect_b64 s[4:5], -1, 0
	v_add3_u32 v23, v38, v23, v40
	v_cndmask_b32_e32 v40, 0, v64, vcc
	v_add3_u32 v27, v76, v27, v78
	v_add3_u32 v29, v77, v29, v79
	v_add3_u32 v31, v80, v31, v64
	v_add3_u32 v32, v81, v32, v65
	s_waitcnt vmcnt(0)
	v_cndmask_b32_e64 v34, 0, v57, s[4:5]
	v_cndmask_b32_e64 v38, 0, v56, s[4:5]
	v_add3_u32 v25, v36, v25, v40
	v_add3_u32 v51, v34, v19, v23
	v_add3_u32 v50, v38, v21, v25
	v_add3_u32 v21, v57, v29, v32
	v_add3_u32 v19, v56, v27, v31
